# v21: lever 2 / 7.3 - attention epilogue stores widened: 16 eight-byte stores per lane per unit (4x4 quad transpose by DPP + v_perm) instead of 64 two-byte stores
# baseline (speedup 1.0000x reference)
.LBB0_646:
	s_or_b64 exec, exec, s[10:11]
	s_waitcnt lgkmcnt(0)
	v_lshl_add_u32 v80, v67, 4, s56
	ds_read_b128 v[72:75], v80
	ds_read_b128 v[76:79], v80 offset:32
	s_lshl_b64 s[8:9], s[22:23], 12
	s_add_u32 s0, s35, s8
	s_addc_u32 s1, s36, s9
	s_lshl_b64 s[8:9], s[14:15], 1
	s_add_u32 s8, s0, s8
	s_addc_u32 s9, s1, s9
	v_and_b32_e32 v81, 3, v66
	v_lshl_add_u32 v82, v67, 2, v81
	v_and_b32_e32 v83, 28, v66
	v_lshlrev_b32_e32 v84, 12, v82
	v_lshl_add_u32 v84, v83, 1, v84
	v_mov_b32_e32 v85, 0
	v_lshl_add_u64 v[82:83], s[8:9], 0, v[84:85]
	v_and_b32_e32 v84, 2, v66
	v_cmp_ne_u32_e32 vcc, 0, v84
	v_and_b32_e32 v84, 1, v66
	v_cmp_ne_u32_e64 s[10:11], 0, v84
	v_mov_b32_e32 v81, 0x5040100
	v_mov_b32_e32 v84, 0x3020706
	s_nop 0
	v_cndmask_b32_e64 v81, v81, v84, s[10:11]
	s_mov_b32 s10, 0x8000
	s_mov_b32 s11, 0
	s_waitcnt lgkmcnt(0)
	v_rcp_f32_e32 v72, v72
	v_rcp_f32_e32 v73, v73
	v_rcp_f32_e32 v74, v74
	v_rcp_f32_e32 v75, v75
	v_rcp_f32_e32 v76, v76
	v_rcp_f32_e32 v77, v77
	v_rcp_f32_e32 v78, v78
	v_rcp_f32_e32 v79, v79
	s_nop 0
	v_mul_f32_e32 v18, v18, v72
	v_mul_f32_e32 v19, v19, v73
	v_mul_f32_e32 v20, v20, v74
	v_mul_f32_e32 v21, v21, v75
	v_cvt_pk_bf16_f32 v18, v18, v19
	v_cvt_pk_bf16_f32 v20, v20, v21
	s_nop 1
	v_mov_b32_dpp v19, v18 quad_perm:[1,0,3,2] row_mask:0xf bank_mask:0xf bound_ctrl:1
	v_mov_b32_dpp v21, v20 quad_perm:[1,0,3,2] row_mask:0xf bank_mask:0xf bound_ctrl:1
	v_perm_b32 v68, v19, v18, v81
	v_perm_b32 v69, v21, v20, v81
	v_cndmask_b32_e32 v18, v68, v69, vcc
	v_cndmask_b32_e32 v19, v69, v68, vcc
	s_nop 1
	v_mov_b32_dpp v20, v19 quad_perm:[2,3,0,1] row_mask:0xf bank_mask:0xf bound_ctrl:1
	v_cndmask_b32_e32 v70, v18, v20, vcc
	v_cndmask_b32_e32 v71, v20, v18, vcc
	global_store_dwordx2 v[82:83], v[70:71], off
	v_mul_f32_e32 v50, v50, v72
	v_mul_f32_e32 v51, v51, v73
	v_mul_f32_e32 v52, v52, v74
	v_mul_f32_e32 v53, v53, v75
	v_cvt_pk_bf16_f32 v50, v50, v51
	v_cvt_pk_bf16_f32 v52, v52, v53
	s_nop 1
	v_mov_b32_dpp v51, v50 quad_perm:[1,0,3,2] row_mask:0xf bank_mask:0xf bound_ctrl:1
	v_mov_b32_dpp v53, v52 quad_perm:[1,0,3,2] row_mask:0xf bank_mask:0xf bound_ctrl:1
	v_perm_b32 v68, v51, v50, v81
	v_perm_b32 v69, v53, v52, v81
	v_cndmask_b32_e32 v50, v68, v69, vcc
	v_cndmask_b32_e32 v51, v69, v68, vcc
	s_nop 1
	v_mov_b32_dpp v52, v51 quad_perm:[2,3,0,1] row_mask:0xf bank_mask:0xf bound_ctrl:1
	v_cndmask_b32_e32 v70, v50, v52, vcc
	v_cndmask_b32_e32 v71, v52, v50, vcc
	global_store_dwordx2 v[82:83], v[70:71], off offset:64
	v_mul_f32_e32 v34, v34, v72
	v_mul_f32_e32 v35, v35, v73
	v_mul_f32_e32 v36, v36, v74
	v_mul_f32_e32 v37, v37, v75
	v_cvt_pk_bf16_f32 v34, v34, v35
	v_cvt_pk_bf16_f32 v36, v36, v37
	s_nop 1
	v_mov_b32_dpp v35, v34 quad_perm:[1,0,3,2] row_mask:0xf bank_mask:0xf bound_ctrl:1
	v_mov_b32_dpp v37, v36 quad_perm:[1,0,3,2] row_mask:0xf bank_mask:0xf bound_ctrl:1
	v_perm_b32 v68, v35, v34, v81
	v_perm_b32 v69, v37, v36, v81
	v_cndmask_b32_e32 v34, v68, v69, vcc
	v_cndmask_b32_e32 v35, v69, v68, vcc
	s_nop 1
	v_mov_b32_dpp v36, v35 quad_perm:[2,3,0,1] row_mask:0xf bank_mask:0xf bound_ctrl:1
	v_cndmask_b32_e32 v70, v34, v36, vcc
	v_cndmask_b32_e32 v71, v36, v34, vcc
	global_store_dwordx2 v[82:83], v[70:71], off offset:128
	v_mul_f32_e32 v2, v2, v72
	v_mul_f32_e32 v3, v3, v73
	v_mul_f32_e32 v4, v4, v74
	v_mul_f32_e32 v5, v5, v75
	v_cvt_pk_bf16_f32 v2, v2, v3
	v_cvt_pk_bf16_f32 v4, v4, v5
	s_nop 1
	v_mov_b32_dpp v3, v2 quad_perm:[1,0,3,2] row_mask:0xf bank_mask:0xf bound_ctrl:1
	v_mov_b32_dpp v5, v4 quad_perm:[1,0,3,2] row_mask:0xf bank_mask:0xf bound_ctrl:1
	v_perm_b32 v68, v3, v2, v81
	v_perm_b32 v69, v5, v4, v81
	v_cndmask_b32_e32 v2, v68, v69, vcc
	v_cndmask_b32_e32 v3, v69, v68, vcc
	s_nop 1
	v_mov_b32_dpp v4, v3 quad_perm:[2,3,0,1] row_mask:0xf bank_mask:0xf bound_ctrl:1
	v_cndmask_b32_e32 v70, v2, v4, vcc
	v_cndmask_b32_e32 v71, v4, v2, vcc
	global_store_dwordx2 v[82:83], v[70:71], off offset:192
	v_lshl_add_u64 v[82:83], v[82:83], 0, s[10:11]
	v_mul_f32_e32 v22, v22, v76
	v_mul_f32_e32 v23, v23, v77
	v_mul_f32_e32 v24, v24, v78
	v_mul_f32_e32 v25, v25, v79
	v_cvt_pk_bf16_f32 v22, v22, v23
	v_cvt_pk_bf16_f32 v24, v24, v25
	s_nop 1
	v_mov_b32_dpp v23, v22 quad_perm:[1,0,3,2] row_mask:0xf bank_mask:0xf bound_ctrl:1
	v_mov_b32_dpp v25, v24 quad_perm:[1,0,3,2] row_mask:0xf bank_mask:0xf bound_ctrl:1
	v_perm_b32 v68, v23, v22, v81
	v_perm_b32 v69, v25, v24, v81
	v_cndmask_b32_e32 v22, v68, v69, vcc
	v_cndmask_b32_e32 v23, v69, v68, vcc
	s_nop 1
	v_mov_b32_dpp v24, v23 quad_perm:[2,3,0,1] row_mask:0xf bank_mask:0xf bound_ctrl:1
	v_cndmask_b32_e32 v70, v22, v24, vcc
	v_cndmask_b32_e32 v71, v24, v22, vcc
	global_store_dwordx2 v[82:83], v[70:71], off
	v_mul_f32_e32 v54, v54, v76
	v_mul_f32_e32 v55, v55, v77
	v_mul_f32_e32 v56, v56, v78
	v_mul_f32_e32 v57, v57, v79
	v_cvt_pk_bf16_f32 v54, v54, v55
	v_cvt_pk_bf16_f32 v56, v56, v57
	s_nop 1
	v_mov_b32_dpp v55, v54 quad_perm:[1,0,3,2] row_mask:0xf bank_mask:0xf bound_ctrl:1
	v_mov_b32_dpp v57, v56 quad_perm:[1,0,3,2] row_mask:0xf bank_mask:0xf bound_ctrl:1
	v_perm_b32 v68, v55, v54, v81
	v_perm_b32 v69, v57, v56, v81
	v_cndmask_b32_e32 v54, v68, v69, vcc
	v_cndmask_b32_e32 v55, v69, v68, vcc
	s_nop 1
	v_mov_b32_dpp v56, v55 quad_perm:[2,3,0,1] row_mask:0xf bank_mask:0xf bound_ctrl:1
	v_cndmask_b32_e32 v70, v54, v56, vcc
	v_cndmask_b32_e32 v71, v56, v54, vcc
	global_store_dwordx2 v[82:83], v[70:71], off offset:64
	v_mul_f32_e32 v38, v38, v76
	v_mul_f32_e32 v39, v39, v77
	v_mul_f32_e32 v40, v40, v78
	v_mul_f32_e32 v41, v41, v79
	v_cvt_pk_bf16_f32 v38, v38, v39
	v_cvt_pk_bf16_f32 v40, v40, v41
	s_nop 1
	v_mov_b32_dpp v39, v38 quad_perm:[1,0,3,2] row_mask:0xf bank_mask:0xf bound_ctrl:1
	v_mov_b32_dpp v41, v40 quad_perm:[1,0,3,2] row_mask:0xf bank_mask:0xf bound_ctrl:1
	v_perm_b32 v68, v39, v38, v81
	v_perm_b32 v69, v41, v40, v81
	v_cndmask_b32_e32 v38, v68, v69, vcc
	v_cndmask_b32_e32 v39, v69, v68, vcc
	s_nop 1
	v_mov_b32_dpp v40, v39 quad_perm:[2,3,0,1] row_mask:0xf bank_mask:0xf bound_ctrl:1
	v_cndmask_b32_e32 v70, v38, v40, vcc
	v_cndmask_b32_e32 v71, v40, v38, vcc
	global_store_dwordx2 v[82:83], v[70:71], off offset:128
	v_mul_f32_e32 v6, v6, v76
	v_mul_f32_e32 v7, v7, v77
	v_mul_f32_e32 v8, v8, v78
	v_mul_f32_e32 v9, v9, v79
	v_cvt_pk_bf16_f32 v6, v6, v7
	v_cvt_pk_bf16_f32 v8, v8, v9
	s_nop 1
	v_mov_b32_dpp v7, v6 quad_perm:[1,0,3,2] row_mask:0xf bank_mask:0xf bound_ctrl:1
	v_mov_b32_dpp v9, v8 quad_perm:[1,0,3,2] row_mask:0xf bank_mask:0xf bound_ctrl:1
	v_perm_b32 v68, v7, v6, v81
	v_perm_b32 v69, v9, v8, v81
	v_cndmask_b32_e32 v6, v68, v69, vcc
	v_cndmask_b32_e32 v7, v69, v68, vcc
	s_nop 1
	v_mov_b32_dpp v8, v7 quad_perm:[2,3,0,1] row_mask:0xf bank_mask:0xf bound_ctrl:1
	v_cndmask_b32_e32 v70, v6, v8, vcc
	v_cndmask_b32_e32 v71, v8, v6, vcc
	global_store_dwordx2 v[82:83], v[70:71], off offset:192
	v_lshl_add_u64 v[82:83], v[82:83], 0, s[10:11]
	ds_read_b128 v[72:75], v80 offset:64
	ds_read_b128 v[76:79], v80 offset:96
	s_waitcnt lgkmcnt(0)
	v_rcp_f32_e32 v72, v72
	v_rcp_f32_e32 v73, v73
	v_rcp_f32_e32 v74, v74
	v_rcp_f32_e32 v75, v75
	v_rcp_f32_e32 v76, v76
	v_rcp_f32_e32 v77, v77
	v_rcp_f32_e32 v78, v78
	v_rcp_f32_e32 v79, v79
	s_nop 0
	v_mul_f32_e32 v26, v26, v72
	v_mul_f32_e32 v27, v27, v73
	v_mul_f32_e32 v28, v28, v74
	v_mul_f32_e32 v29, v29, v75
	v_cvt_pk_bf16_f32 v26, v26, v27
	v_cvt_pk_bf16_f32 v28, v28, v29
	s_nop 1
	v_mov_b32_dpp v27, v26 quad_perm:[1,0,3,2] row_mask:0xf bank_mask:0xf bound_ctrl:1
	v_mov_b32_dpp v29, v28 quad_perm:[1,0,3,2] row_mask:0xf bank_mask:0xf bound_ctrl:1
	v_perm_b32 v68, v27, v26, v81
	v_perm_b32 v69, v29, v28, v81
	v_cndmask_b32_e32 v26, v68, v69, vcc
	v_cndmask_b32_e32 v27, v69, v68, vcc
	s_nop 1
	v_mov_b32_dpp v28, v27 quad_perm:[2,3,0,1] row_mask:0xf bank_mask:0xf bound_ctrl:1
	v_cndmask_b32_e32 v70, v26, v28, vcc
	v_cndmask_b32_e32 v71, v28, v26, vcc
	global_store_dwordx2 v[82:83], v[70:71], off
	v_mul_f32_e32 v58, v58, v72
	v_mul_f32_e32 v59, v59, v73
	v_mul_f32_e32 v60, v60, v74
	v_mul_f32_e32 v61, v61, v75
	v_cvt_pk_bf16_f32 v58, v58, v59
	v_cvt_pk_bf16_f32 v60, v60, v61
	s_nop 1
	v_mov_b32_dpp v59, v58 quad_perm:[1,0,3,2] row_mask:0xf bank_mask:0xf bound_ctrl:1
	v_mov_b32_dpp v61, v60 quad_perm:[1,0,3,2] row_mask:0xf bank_mask:0xf bound_ctrl:1
	v_perm_b32 v68, v59, v58, v81
	v_perm_b32 v69, v61, v60, v81
	v_cndmask_b32_e32 v58, v68, v69, vcc
	v_cndmask_b32_e32 v59, v69, v68, vcc
	s_nop 1
	v_mov_b32_dpp v60, v59 quad_perm:[2,3,0,1] row_mask:0xf bank_mask:0xf bound_ctrl:1
	v_cndmask_b32_e32 v70, v58, v60, vcc
	v_cndmask_b32_e32 v71, v60, v58, vcc
	global_store_dwordx2 v[82:83], v[70:71], off offset:64
	v_mul_f32_e32 v42, v42, v72
	v_mul_f32_e32 v43, v43, v73
	v_mul_f32_e32 v44, v44, v74
	v_mul_f32_e32 v45, v45, v75
	v_cvt_pk_bf16_f32 v42, v42, v43
	v_cvt_pk_bf16_f32 v44, v44, v45
	s_nop 1
	v_mov_b32_dpp v43, v42 quad_perm:[1,0,3,2] row_mask:0xf bank_mask:0xf bound_ctrl:1
	v_mov_b32_dpp v45, v44 quad_perm:[1,0,3,2] row_mask:0xf bank_mask:0xf bound_ctrl:1
	v_perm_b32 v68, v43, v42, v81
	v_perm_b32 v69, v45, v44, v81
	v_cndmask_b32_e32 v42, v68, v69, vcc
	v_cndmask_b32_e32 v43, v69, v68, vcc
	s_nop 1
	v_mov_b32_dpp v44, v43 quad_perm:[2,3,0,1] row_mask:0xf bank_mask:0xf bound_ctrl:1
	v_cndmask_b32_e32 v70, v42, v44, vcc
	v_cndmask_b32_e32 v71, v44, v42, vcc
	global_store_dwordx2 v[82:83], v[70:71], off offset:128
	v_mul_f32_e32 v10, v10, v72
	v_mul_f32_e32 v11, v11, v73
	v_mul_f32_e32 v12, v12, v74
	v_mul_f32_e32 v13, v13, v75
	v_cvt_pk_bf16_f32 v10, v10, v11
	v_cvt_pk_bf16_f32 v12, v12, v13
	s_nop 1
	v_mov_b32_dpp v11, v10 quad_perm:[1,0,3,2] row_mask:0xf bank_mask:0xf bound_ctrl:1
	v_mov_b32_dpp v13, v12 quad_perm:[1,0,3,2] row_mask:0xf bank_mask:0xf bound_ctrl:1
	v_perm_b32 v68, v11, v10, v81
	v_perm_b32 v69, v13, v12, v81
	v_cndmask_b32_e32 v10, v68, v69, vcc
	v_cndmask_b32_e32 v11, v69, v68, vcc
	s_nop 1
	v_mov_b32_dpp v12, v11 quad_perm:[2,3,0,1] row_mask:0xf bank_mask:0xf bound_ctrl:1
	v_cndmask_b32_e32 v70, v10, v12, vcc
	v_cndmask_b32_e32 v71, v12, v10, vcc
	global_store_dwordx2 v[82:83], v[70:71], off offset:192
	v_lshl_add_u64 v[82:83], v[82:83], 0, s[10:11]
	v_mul_f32_e32 v30, v30, v76
	v_mul_f32_e32 v31, v31, v77
	v_mul_f32_e32 v32, v32, v78
	v_mul_f32_e32 v33, v33, v79
	v_cvt_pk_bf16_f32 v30, v30, v31
	v_cvt_pk_bf16_f32 v32, v32, v33
	s_nop 1
	v_mov_b32_dpp v31, v30 quad_perm:[1,0,3,2] row_mask:0xf bank_mask:0xf bound_ctrl:1
	v_mov_b32_dpp v33, v32 quad_perm:[1,0,3,2] row_mask:0xf bank_mask:0xf bound_ctrl:1
	v_perm_b32 v68, v31, v30, v81
	v_perm_b32 v69, v33, v32, v81
	v_cndmask_b32_e32 v30, v68, v69, vcc
	v_cndmask_b32_e32 v31, v69, v68, vcc
	s_nop 1
	v_mov_b32_dpp v32, v31 quad_perm:[2,3,0,1] row_mask:0xf bank_mask:0xf bound_ctrl:1
	v_cndmask_b32_e32 v70, v30, v32, vcc
	v_cndmask_b32_e32 v71, v32, v30, vcc
	global_store_dwordx2 v[82:83], v[70:71], off
	v_mul_f32_e32 v62, v62, v76
	v_mul_f32_e32 v63, v63, v77
	v_mul_f32_e32 v64, v64, v78
	v_mul_f32_e32 v65, v65, v79
	v_cvt_pk_bf16_f32 v62, v62, v63
	v_cvt_pk_bf16_f32 v64, v64, v65
	s_nop 1
	v_mov_b32_dpp v63, v62 quad_perm:[1,0,3,2] row_mask:0xf bank_mask:0xf bound_ctrl:1
	v_mov_b32_dpp v65, v64 quad_perm:[1,0,3,2] row_mask:0xf bank_mask:0xf bound_ctrl:1
	v_perm_b32 v68, v63, v62, v81
	v_perm_b32 v69, v65, v64, v81
	v_cndmask_b32_e32 v62, v68, v69, vcc
	v_cndmask_b32_e32 v63, v69, v68, vcc
	s_nop 1
	v_mov_b32_dpp v64, v63 quad_perm:[2,3,0,1] row_mask:0xf bank_mask:0xf bound_ctrl:1
	v_cndmask_b32_e32 v70, v62, v64, vcc
	v_cndmask_b32_e32 v71, v64, v62, vcc
	global_store_dwordx2 v[82:83], v[70:71], off offset:64
	v_mul_f32_e32 v46, v46, v76
	v_mul_f32_e32 v47, v47, v77
	v_mul_f32_e32 v48, v48, v78
	v_mul_f32_e32 v49, v49, v79
	v_cvt_pk_bf16_f32 v46, v46, v47
	v_cvt_pk_bf16_f32 v48, v48, v49
	s_nop 1
	v_mov_b32_dpp v47, v46 quad_perm:[1,0,3,2] row_mask:0xf bank_mask:0xf bound_ctrl:1
	v_mov_b32_dpp v49, v48 quad_perm:[1,0,3,2] row_mask:0xf bank_mask:0xf bound_ctrl:1
	v_perm_b32 v68, v47, v46, v81
	v_perm_b32 v69, v49, v48, v81
	v_cndmask_b32_e32 v46, v68, v69, vcc
	v_cndmask_b32_e32 v47, v69, v68, vcc
	s_nop 1
	v_mov_b32_dpp v48, v47 quad_perm:[2,3,0,1] row_mask:0xf bank_mask:0xf bound_ctrl:1
	v_cndmask_b32_e32 v70, v46, v48, vcc
	v_cndmask_b32_e32 v71, v48, v46, vcc
	global_store_dwordx2 v[82:83], v[70:71], off offset:128
	v_mul_f32_e32 v14, v14, v76
	v_mul_f32_e32 v15, v15, v77
	v_mul_f32_e32 v16, v16, v78
	v_mul_f32_e32 v17, v17, v79
	v_cvt_pk_bf16_f32 v14, v14, v15
	v_cvt_pk_bf16_f32 v16, v16, v17
	s_nop 1
	v_mov_b32_dpp v15, v14 quad_perm:[1,0,3,2] row_mask:0xf bank_mask:0xf bound_ctrl:1
	v_mov_b32_dpp v17, v16 quad_perm:[1,0,3,2] row_mask:0xf bank_mask:0xf bound_ctrl:1
	v_perm_b32 v68, v15, v14, v81
	v_perm_b32 v69, v17, v16, v81
	v_cndmask_b32_e32 v14, v68, v69, vcc
	v_cndmask_b32_e32 v15, v69, v68, vcc
	s_nop 1
	v_mov_b32_dpp v16, v15 quad_perm:[2,3,0,1] row_mask:0xf bank_mask:0xf bound_ctrl:1
	v_cndmask_b32_e32 v70, v14, v16, vcc
	v_cndmask_b32_e32 v71, v16, v14, vcc
	global_store_dwordx2 v[82:83], v[70:71], off offset:192
	s_and_saveexec_b64 s[8:9], s[4:5]
	s_cbranch_execz .LBB0_575
	v_mov_b32_e32 v2, s40
	ds_write_b32 v2, v209
	s_branch .LBB0_575
